# best version plus back-edge rotation of the compute scan loop (branch taken before the step barrier)
# baseline (speedup 1.0000x reference)
.LBB1_6:
	v_mov_b32_e32 v2, 0x7f61b1e6
	v_mov_b32_e32 v195, 0x7f800000
	s_mov_b32 s10, -2
	v_mov_b32_e32 v114, v188
	s_mov_b32 s11, 32
	v_mov_b32_e32 v196, 0x7f800000
	v_mov_b32_e32 v197, 0x7f800000
	v_mov_b32_e32 v198, 0x7f800000
	v_mov_b32_e32 v3, v2
	v_mov_b32_e32 v4, v2
	v_mov_b32_e32 v5, v2
	v_mov_b32_e32 v6, v2
	v_mov_b32_e32 v7, v2
	v_mov_b32_e32 v8, v2
	v_mov_b32_e32 v9, v2
	v_mov_b32_e32 v10, v2
	v_mov_b32_e32 v11, v2
	v_mov_b32_e32 v12, v2
	v_mov_b32_e32 v13, v2
	v_mov_b32_e32 v14, v2
	v_mov_b32_e32 v15, v2
	v_mov_b32_e32 v16, v2
	v_mov_b32_e32 v17, v2
	s_branch .LBB1_7

.LBB1_7:
	ds_read_b128 v[116:119], v181
	ds_read_b128 v[18:21], v114
	ds_read_b128 v[22:25], v114 offset:32
	ds_read_b128 v[26:29], v114 offset:64
	ds_read_b128 v[30:33], v114 offset:96
	ds_read_b128 v[120:123], v181 offset:1024
	ds_read_b128 v[124:127], v181 offset:2048
	ds_read_b128 v[128:131], v181 offset:3072
	s_waitcnt lgkmcnt(3)
	v_mfma_f32_32x32x16_f16 v[18:33], v[116:119], v[94:97], v[18:33]
	ds_read_b128 v[116:119], v181 offset:4096
	s_mov_b32 s28, s3
	s_nop 0
	v_and_or_b32 v2, v2, v177, s28
	v_med3_f32 v115, v196, v195, v2
	v_med3_f32 v136, v197, v196, v2
	v_med3_f32 v137, v198, v197, v2
	v_med3_f32 v2, v198, v2, s42
	ds_read_b128 v[132:135], v181 offset:5120
	s_add_i32 s28, s3, 1
	s_waitcnt lgkmcnt(4)
	v_mfma_f32_32x32x16_f16 v[18:33], v[120:123], v[90:93], v[18:33]
	v_and_or_b32 v3, v3, v177, s28
	v_med3_f32 v115, v136, v115, v3
	v_med3_f32 v136, v137, v136, v3
	v_med3_f32 v137, v2, v137, v3
	v_med3_f32 v2, v2, v3, s42
	ds_read_b128 v[120:123], v181 offset:6144
	s_add_i32 s28, s3, 2
	s_waitcnt lgkmcnt(4)
	v_mfma_f32_32x32x16_f16 v[18:33], v[124:127], v[86:89], v[18:33]
	v_and_or_b32 v3, v4, v177, s28
	v_med3_f32 v4, v136, v115, v3
	v_med3_f32 v115, v137, v136, v3
	v_med3_f32 v136, v2, v137, v3
	v_med3_f32 v2, v2, v3, s42
	ds_read_b128 v[124:127], v181 offset:7168
	s_add_i32 s28, s3, 3
	s_waitcnt lgkmcnt(4)
	v_mfma_f32_32x32x16_f16 v[18:33], v[128:131], v[82:85], v[18:33]
	v_and_or_b32 v3, v5, v177, s28
	v_med3_f32 v137, v115, v4, v3
	v_med3_f32 v115, v136, v115, v3
	v_med3_f32 v128, v2, v136, v3
	v_med3_f32 v129, v2, v3, s42
	ds_read_b128 v[2:5], v181 offset:8192
	s_add_i32 s28, s3, 4
	s_waitcnt lgkmcnt(4)
	v_mfma_f32_32x32x16_f16 v[18:33], v[116:119], v[78:81], v[18:33]
	v_and_or_b32 v6, v6, v177, s28
	v_med3_f32 v130, v115, v137, v6
	v_med3_f32 v115, v128, v115, v6
	v_med3_f32 v128, v129, v128, v6
	v_med3_f32 v6, v129, v6, s42
	ds_read_b128 v[116:119], v181 offset:9216
	s_add_i32 s28, s3, 5
	s_waitcnt lgkmcnt(4)
	v_mfma_f32_32x32x16_f16 v[18:33], v[132:135], v[74:77], v[18:33]
	v_and_or_b32 v7, v7, v177, s28
	v_med3_f32 v132, v6, v128, v7
	v_med3_f32 v6, v6, v7, s42
	v_med3_f32 v136, v115, v130, v7
	v_med3_f32 v115, v128, v115, v7
	ds_read_b128 v[128:131], v181 offset:10240
	s_add_i32 s28, s3, 6
	s_waitcnt lgkmcnt(4)
	v_mfma_f32_32x32x16_f16 v[18:33], v[120:123], v[70:73], v[18:33]
	v_and_or_b32 v7, v8, v177, s28
	v_med3_f32 v8, v115, v136, v7
	v_med3_f32 v115, v132, v115, v7
	v_med3_f32 v132, v6, v132, v7
	v_med3_f32 v6, v6, v7, s42
	ds_read_b128 v[120:123], v181 offset:11264
	s_add_i32 s28, s3, 7
	s_waitcnt lgkmcnt(4)
	v_mfma_f32_32x32x16_f16 v[18:33], v[124:127], v[66:69], v[18:33]
	v_and_or_b32 v7, v9, v177, s28
	v_med3_f32 v133, v115, v8, v7
	v_med3_f32 v115, v132, v115, v7
	v_med3_f32 v124, v6, v132, v7
	v_med3_f32 v125, v6, v7, s42
	ds_read_b128 v[6:9], v181 offset:12288
	s_add_i32 s28, s3, 8
	s_waitcnt lgkmcnt(4)
	v_mfma_f32_32x32x16_f16 v[18:33], v[2:5], v[62:65], v[18:33]
	v_and_or_b32 v10, v10, v177, s28
	v_med3_f32 v126, v115, v133, v10
	v_med3_f32 v115, v124, v115, v10
	v_med3_f32 v124, v125, v124, v10
	v_med3_f32 v10, v125, v10, s42
	ds_read_b128 v[2:5], v181 offset:13312
	s_add_i32 s28, s3, 9
	s_waitcnt lgkmcnt(4)
	v_mfma_f32_32x32x16_f16 v[18:33], v[116:119], v[58:61], v[18:33]
	v_and_or_b32 v11, v11, v177, s28
	v_med3_f32 v125, v115, v126, v11
	v_med3_f32 v115, v124, v115, v11
	v_med3_f32 v124, v10, v124, v11
	v_med3_f32 v10, v10, v11, s42
	ds_read_b128 v[116:119], v181 offset:14336
	s_add_i32 s28, s3, 10
	s_waitcnt lgkmcnt(4)
	v_mfma_f32_32x32x16_f16 v[18:33], v[128:131], v[54:57], v[18:33]
	v_and_or_b32 v11, v12, v177, s28
	v_med3_f32 v12, v115, v125, v11
	v_med3_f32 v128, v10, v124, v11
	v_med3_f32 v10, v10, v11, s42
	v_med3_f32 v115, v124, v115, v11
	ds_read_b128 v[124:127], v181 offset:15360
	s_add_i32 s28, s3, 11
	s_waitcnt lgkmcnt(4)
	v_mfma_f32_32x32x16_f16 v[18:33], v[120:123], v[50:53], v[18:33]
	v_and_or_b32 v11, v13, v177, s28
	v_med3_f32 v12, v115, v12, v11
	v_med3_f32 v13, v128, v115, v11
	v_med3_f32 v115, v10, v128, v11
	v_med3_f32 v10, v10, v11, s42
	s_add_i32 s28, s3, 12
	s_waitcnt lgkmcnt(3)
	v_mfma_f32_32x32x16_f16 v[18:33], v[6:9], v[46:49], v[18:33]
	v_and_or_b32 v11, v14, v177, s28
	v_med3_f32 v12, v13, v12, v11
	v_med3_f32 v13, v115, v13, v11
	v_med3_f32 v14, v10, v115, v11
	v_med3_f32 v6, v10, v11, s42
	s_add_i32 s28, s3, 13
	s_waitcnt lgkmcnt(2)
	v_mfma_f32_32x32x16_f16 v[18:33], v[2:5], v[42:45], v[18:33]
	v_and_or_b32 v7, v15, v177, s28
	v_med3_f32 v8, v13, v12, v7
	v_med3_f32 v9, v14, v13, v7
	v_med3_f32 v10, v6, v14, v7
	v_med3_f32 v2, v6, v7, s42
	s_add_i32 s28, s3, 14
	s_waitcnt lgkmcnt(1)
	v_mfma_f32_32x32x16_f16 v[18:33], v[116:119], v[38:41], v[18:33]
	v_and_or_b32 v3, v16, v177, s28
	v_med3_f32 v4, v9, v8, v3
	v_med3_f32 v5, v10, v9, v3
	v_med3_f32 v6, v2, v10, v3
	v_med3_f32 v2, v2, v3, s42
	s_add_i32 s3, s3, 15
	s_waitcnt lgkmcnt(0)
	v_mfma_f32_32x32x16_f16 v[18:33], v[124:127], v[34:37], v[18:33]
	v_and_or_b32 v3, v17, v177, s3
	v_med3_f32 v115, v5, v4, v3
	v_med3_f32 v132, v6, v5, v3
	v_med3_f32 v133, v2, v6, v3
	v_med3_f32 v134, v2, v3, s42
	ds_read_b128 v[116:119], v181 offset:16384
	ds_read_b128 v[2:5], v114 offset:128
	ds_read_b128 v[6:9], v114 offset:160
	ds_read_b128 v[10:13], v114 offset:192
	ds_read_b128 v[14:17], v114 offset:224
	ds_read_b128 v[120:123], v181 offset:17408
	ds_read_b128 v[124:127], v181 offset:18432
	ds_read_b128 v[128:131], v181 offset:19456
	s_sub_i32 s3, s11, 32
	s_waitcnt lgkmcnt(3)
	v_mfma_f32_32x32x16_f16 v[2:17], v[116:119], v[94:97], v[2:17]
	ds_read_b128 v[116:119], v181 offset:20480
	s_mov_b32 s28, s3
	s_nop 0
	v_and_or_b32 v18, v18, v177, s28
	v_med3_f32 v115, v132, v115, v18
	v_med3_f32 v136, v133, v132, v18
	v_med3_f32 v137, v134, v133, v18
	v_med3_f32 v18, v134, v18, s42
	s_waitcnt lgkmcnt(3)
	v_mfma_f32_32x32x16_f16 v[2:17], v[120:123], v[90:93], v[2:17]
	ds_read_b128 v[132:135], v181 offset:21504
	s_add_i32 s28, s3, 1
	s_nop 0
	v_and_or_b32 v19, v19, v177, s28
	v_med3_f32 v115, v136, v115, v19
	v_med3_f32 v136, v137, v136, v19
	v_med3_f32 v137, v18, v137, v19
	v_med3_f32 v18, v18, v19, s42
	s_waitcnt lgkmcnt(3)
	v_mfma_f32_32x32x16_f16 v[2:17], v[124:127], v[86:89], v[2:17]
	ds_read_b128 v[120:123], v181 offset:22528
	s_add_i32 s28, s3, 2
	s_nop 0
	v_and_or_b32 v19, v20, v177, s28
	v_med3_f32 v20, v136, v115, v19
	v_med3_f32 v115, v137, v136, v19
	v_med3_f32 v136, v18, v137, v19
	v_med3_f32 v18, v18, v19, s42
	s_waitcnt lgkmcnt(3)
	v_mfma_f32_32x32x16_f16 v[2:17], v[128:131], v[82:85], v[2:17]
	ds_read_b128 v[124:127], v181 offset:23552
	s_add_i32 s28, s3, 3
	s_nop 0
	v_and_or_b32 v19, v21, v177, s28
	v_med3_f32 v137, v115, v20, v19
	v_med3_f32 v115, v136, v115, v19
	v_med3_f32 v128, v18, v136, v19
	v_med3_f32 v129, v18, v19, s42
	s_waitcnt lgkmcnt(3)
	v_mfma_f32_32x32x16_f16 v[2:17], v[116:119], v[78:81], v[2:17]
	ds_read_b128 v[18:21], v181 offset:24576
	s_add_i32 s28, s3, 4
	s_nop 0
	v_and_or_b32 v22, v22, v177, s28
	v_med3_f32 v130, v115, v137, v22
	v_med3_f32 v115, v128, v115, v22
	v_med3_f32 v128, v129, v128, v22
	v_med3_f32 v22, v129, v22, s42
	s_waitcnt lgkmcnt(3)
	v_mfma_f32_32x32x16_f16 v[2:17], v[132:135], v[74:77], v[2:17]
	ds_read_b128 v[116:119], v181 offset:25600
	s_add_i32 s28, s3, 5
	s_nop 0
	v_and_or_b32 v23, v23, v177, s28
	v_med3_f32 v136, v115, v130, v23
	v_med3_f32 v115, v128, v115, v23
	v_med3_f32 v132, v22, v128, v23
	v_med3_f32 v22, v22, v23, s42
	s_waitcnt lgkmcnt(3)
	v_mfma_f32_32x32x16_f16 v[2:17], v[120:123], v[70:73], v[2:17]
	ds_read_b128 v[128:131], v181 offset:26624
	s_add_i32 s28, s3, 6
	s_nop 0
	v_and_or_b32 v23, v24, v177, s28
	v_med3_f32 v24, v115, v136, v23
	v_med3_f32 v115, v132, v115, v23
	v_med3_f32 v132, v22, v132, v23
	v_med3_f32 v22, v22, v23, s42
	s_waitcnt lgkmcnt(3)
	v_mfma_f32_32x32x16_f16 v[2:17], v[124:127], v[66:69], v[2:17]
	ds_read_b128 v[120:123], v181 offset:27648
	s_add_i32 s28, s3, 7
	s_nop 0
	v_and_or_b32 v23, v25, v177, s28
	v_med3_f32 v133, v115, v24, v23
	v_med3_f32 v115, v132, v115, v23
	v_med3_f32 v124, v22, v132, v23
	v_med3_f32 v125, v22, v23, s42
	s_waitcnt lgkmcnt(3)
	v_mfma_f32_32x32x16_f16 v[2:17], v[18:21], v[62:65], v[2:17]
	ds_read_b128 v[22:25], v181 offset:28672
	s_add_i32 s28, s3, 8
	s_nop 0
	v_and_or_b32 v26, v26, v177, s28
	v_med3_f32 v126, v115, v133, v26
	v_med3_f32 v115, v124, v115, v26
	v_med3_f32 v124, v125, v124, v26
	v_med3_f32 v26, v125, v26, s42
	s_waitcnt lgkmcnt(3)
	v_mfma_f32_32x32x16_f16 v[2:17], v[116:119], v[58:61], v[2:17]
	ds_read_b128 v[18:21], v181 offset:29696
	s_add_i32 s28, s3, 9
	s_nop 0
	v_and_or_b32 v27, v27, v177, s28
	v_med3_f32 v125, v115, v126, v27
	v_med3_f32 v115, v124, v115, v27
	v_med3_f32 v124, v26, v124, v27
	v_med3_f32 v26, v26, v27, s42
	s_waitcnt lgkmcnt(3)
	v_mfma_f32_32x32x16_f16 v[2:17], v[128:131], v[54:57], v[2:17]
	ds_read_b128 v[116:119], v181 offset:30720
	s_add_i32 s28, s3, 10
	s_nop 0
	v_and_or_b32 v27, v28, v177, s28
	v_med3_f32 v28, v115, v125, v27
	v_med3_f32 v115, v124, v115, v27
	v_med3_f32 v128, v26, v124, v27
	v_med3_f32 v26, v26, v27, s42
	s_waitcnt lgkmcnt(3)
	v_mfma_f32_32x32x16_f16 v[2:17], v[120:123], v[50:53], v[2:17]
	ds_read_b128 v[124:127], v181 offset:31744
	s_add_i32 s28, s3, 11
	s_nop 0
	v_and_or_b32 v27, v29, v177, s28
	v_med3_f32 v28, v115, v28, v27
	v_med3_f32 v29, v128, v115, v27
	v_med3_f32 v115, v26, v128, v27
	v_med3_f32 v26, v26, v27, s42
	s_waitcnt lgkmcnt(3)
	v_mfma_f32_32x32x16_f16 v[2:17], v[22:25], v[46:49], v[2:17]
	s_add_i32 s28, s3, 12
	s_nop 0
	v_and_or_b32 v27, v30, v177, s28
	v_med3_f32 v28, v29, v28, v27
	v_med3_f32 v29, v115, v29, v27
	v_med3_f32 v30, v26, v115, v27
	v_med3_f32 v22, v26, v27, s42
	s_waitcnt lgkmcnt(2)
	v_mfma_f32_32x32x16_f16 v[2:17], v[18:21], v[42:45], v[2:17]
	s_add_i32 s28, s3, 13
	s_nop 0
	v_and_or_b32 v23, v31, v177, s28
	v_med3_f32 v24, v29, v28, v23
	v_med3_f32 v25, v30, v29, v23
	v_med3_f32 v26, v22, v30, v23
	v_med3_f32 v18, v22, v23, s42
	s_waitcnt lgkmcnt(1)
	v_mfma_f32_32x32x16_f16 v[2:17], v[116:119], v[38:41], v[2:17]
	s_add_i32 s28, s3, 14
	s_nop 0
	v_and_or_b32 v19, v32, v177, s28
	v_med3_f32 v20, v25, v24, v19
	v_med3_f32 v21, v26, v25, v19
	v_med3_f32 v22, v18, v26, v19
	v_med3_f32 v18, v18, v19, s42
	s_waitcnt lgkmcnt(0)
	v_mfma_f32_32x32x16_f16 v[2:17], v[124:127], v[34:37], v[2:17]
	s_add_i32 s3, s3, 15
	s_nop 0
	v_and_or_b32 v19, v33, v177, s3
	v_med3_f32 v115, v21, v20, v19
	v_med3_f32 v132, v22, v21, v19
	v_med3_f32 v133, v18, v22, v19
	v_med3_f32 v134, v18, v19, s42
	s_barrier
	ds_read_b128 v[116:119], v181 offset:32768
	ds_read_b128 v[18:21], v114 offset:256
	ds_read_b128 v[22:25], v114 offset:288
	ds_read_b128 v[26:29], v114 offset:320
	ds_read_b128 v[30:33], v114 offset:352
	ds_read_b128 v[120:123], v181 offset:33792
	ds_read_b128 v[124:127], v181 offset:34816
	ds_read_b128 v[128:131], v181 offset:35840
	s_add_i32 s3, s11, -16
	s_waitcnt lgkmcnt(3)
	v_mfma_f32_32x32x16_f16 v[18:33], v[116:119], v[94:97], v[18:33]
	ds_read_b128 v[116:119], v181 offset:36864
	s_mov_b32 s28, s3
	s_nop 0
	v_and_or_b32 v2, v2, v177, s28
	v_med3_f32 v115, v132, v115, v2
	v_med3_f32 v136, v133, v132, v2
	v_med3_f32 v137, v134, v133, v2
	v_med3_f32 v2, v134, v2, s42
	ds_read_b128 v[132:135], v181 offset:37888
	s_add_i32 s28, s3, 1
	s_waitcnt lgkmcnt(4)
	v_mfma_f32_32x32x16_f16 v[18:33], v[120:123], v[90:93], v[18:33]
	v_and_or_b32 v3, v3, v177, s28
	v_med3_f32 v115, v136, v115, v3
	v_med3_f32 v136, v137, v136, v3
	v_med3_f32 v137, v2, v137, v3
	v_med3_f32 v2, v2, v3, s42
	ds_read_b128 v[120:123], v181 offset:38912
	s_add_i32 s28, s3, 2
	s_waitcnt lgkmcnt(4)
	v_mfma_f32_32x32x16_f16 v[18:33], v[124:127], v[86:89], v[18:33]
	v_and_or_b32 v3, v4, v177, s28
	v_med3_f32 v4, v136, v115, v3
	v_med3_f32 v115, v137, v136, v3
	v_med3_f32 v136, v2, v137, v3
	v_med3_f32 v2, v2, v3, s42
	ds_read_b128 v[124:127], v181 offset:39936
	s_add_i32 s28, s3, 3
	s_waitcnt lgkmcnt(4)
	v_mfma_f32_32x32x16_f16 v[18:33], v[128:131], v[82:85], v[18:33]
	v_and_or_b32 v3, v5, v177, s28
	v_med3_f32 v137, v115, v4, v3
	v_med3_f32 v115, v136, v115, v3
	v_med3_f32 v128, v2, v136, v3
	v_med3_f32 v129, v2, v3, s42
	ds_read_b128 v[2:5], v181 offset:40960
	s_add_i32 s28, s3, 4
	s_waitcnt lgkmcnt(4)
	v_mfma_f32_32x32x16_f16 v[18:33], v[116:119], v[78:81], v[18:33]
	v_and_or_b32 v6, v6, v177, s28
	v_med3_f32 v130, v115, v137, v6
	v_med3_f32 v115, v128, v115, v6
	v_med3_f32 v128, v129, v128, v6
	v_med3_f32 v6, v129, v6, s42
	ds_read_b128 v[116:119], v181 offset:41984
	s_add_i32 s28, s3, 5
	s_waitcnt lgkmcnt(4)
	v_mfma_f32_32x32x16_f16 v[18:33], v[132:135], v[74:77], v[18:33]
	v_and_or_b32 v7, v7, v177, s28
	v_med3_f32 v132, v6, v128, v7
	v_med3_f32 v6, v6, v7, s42
	v_med3_f32 v136, v115, v130, v7
	v_med3_f32 v115, v128, v115, v7
	ds_read_b128 v[128:131], v181 offset:43008
	s_add_i32 s28, s3, 6
	s_waitcnt lgkmcnt(4)
	v_mfma_f32_32x32x16_f16 v[18:33], v[120:123], v[70:73], v[18:33]
	v_and_or_b32 v7, v8, v177, s28
	v_med3_f32 v8, v115, v136, v7
	v_med3_f32 v115, v132, v115, v7
	v_med3_f32 v132, v6, v132, v7
	v_med3_f32 v6, v6, v7, s42
	ds_read_b128 v[120:123], v181 offset:44032
	s_add_i32 s28, s3, 7
	s_waitcnt lgkmcnt(4)
	v_mfma_f32_32x32x16_f16 v[18:33], v[124:127], v[66:69], v[18:33]
	v_and_or_b32 v7, v9, v177, s28
	v_med3_f32 v133, v115, v8, v7
	v_med3_f32 v115, v132, v115, v7
	v_med3_f32 v124, v6, v132, v7
	v_med3_f32 v125, v6, v7, s42
	ds_read_b128 v[6:9], v181 offset:45056
	s_add_i32 s28, s3, 8
	s_waitcnt lgkmcnt(4)
	v_mfma_f32_32x32x16_f16 v[18:33], v[2:5], v[62:65], v[18:33]
	v_and_or_b32 v10, v10, v177, s28
	v_med3_f32 v126, v115, v133, v10
	v_med3_f32 v115, v124, v115, v10
	v_med3_f32 v124, v125, v124, v10
	v_med3_f32 v10, v125, v10, s42
	ds_read_b128 v[2:5], v181 offset:46080
	s_add_i32 s28, s3, 9
	s_waitcnt lgkmcnt(4)
	v_mfma_f32_32x32x16_f16 v[18:33], v[116:119], v[58:61], v[18:33]
	v_and_or_b32 v11, v11, v177, s28
	v_med3_f32 v125, v115, v126, v11
	v_med3_f32 v115, v124, v115, v11
	v_med3_f32 v124, v10, v124, v11
	v_med3_f32 v10, v10, v11, s42
	ds_read_b128 v[116:119], v181 offset:47104
	s_add_i32 s28, s3, 10
	s_waitcnt lgkmcnt(4)
	v_mfma_f32_32x32x16_f16 v[18:33], v[128:131], v[54:57], v[18:33]
	v_and_or_b32 v11, v12, v177, s28
	v_med3_f32 v12, v115, v125, v11
	v_med3_f32 v128, v10, v124, v11
	v_med3_f32 v10, v10, v11, s42
	v_med3_f32 v115, v124, v115, v11
	ds_read_b128 v[124:127], v181 offset:48128
	s_add_i32 s28, s3, 11
	s_waitcnt lgkmcnt(4)
	v_mfma_f32_32x32x16_f16 v[18:33], v[120:123], v[50:53], v[18:33]
	v_and_or_b32 v11, v13, v177, s28
	v_med3_f32 v12, v115, v12, v11
	v_med3_f32 v13, v128, v115, v11
	v_med3_f32 v115, v10, v128, v11
	v_med3_f32 v10, v10, v11, s42
	s_add_i32 s28, s3, 12
	s_waitcnt lgkmcnt(3)
	v_mfma_f32_32x32x16_f16 v[18:33], v[6:9], v[46:49], v[18:33]
	v_and_or_b32 v11, v14, v177, s28
	v_med3_f32 v12, v13, v12, v11
	v_med3_f32 v13, v115, v13, v11
	v_med3_f32 v14, v10, v115, v11
	v_med3_f32 v6, v10, v11, s42
	s_add_i32 s28, s3, 13
	s_waitcnt lgkmcnt(2)
	v_mfma_f32_32x32x16_f16 v[18:33], v[2:5], v[42:45], v[18:33]
	v_and_or_b32 v7, v15, v177, s28
	v_med3_f32 v8, v13, v12, v7
	v_med3_f32 v9, v14, v13, v7
	v_med3_f32 v10, v6, v14, v7
	v_med3_f32 v2, v6, v7, s42
	s_add_i32 s28, s3, 14
	s_waitcnt lgkmcnt(1)
	v_mfma_f32_32x32x16_f16 v[18:33], v[116:119], v[38:41], v[18:33]
	v_and_or_b32 v3, v16, v177, s28
	v_med3_f32 v4, v9, v8, v3
	v_med3_f32 v5, v10, v9, v3
	v_med3_f32 v6, v2, v10, v3
	v_med3_f32 v2, v2, v3, s42
	s_add_i32 s3, s3, 15
	s_waitcnt lgkmcnt(0)
	v_mfma_f32_32x32x16_f16 v[18:33], v[124:127], v[34:37], v[18:33]
	v_and_or_b32 v3, v17, v177, s3
	v_med3_f32 v115, v5, v4, v3
	v_med3_f32 v132, v6, v5, v3
	v_med3_f32 v133, v2, v6, v3
	v_med3_f32 v134, v2, v3, s42
	ds_read_b128 v[116:119], v181 offset:49152
	ds_read_b128 v[2:5], v114 offset:384
	ds_read_b128 v[6:9], v114 offset:416
	ds_read_b128 v[10:13], v114 offset:448
	ds_read_b128 v[14:17], v114 offset:480
	ds_read_b128 v[120:123], v181 offset:50176
	ds_read_b128 v[124:127], v181 offset:51200
	ds_read_b128 v[128:131], v181 offset:52224
	s_mov_b32 s3, s11
	s_waitcnt lgkmcnt(3)
	v_mfma_f32_32x32x16_f16 v[2:17], v[116:119], v[94:97], v[2:17]
	ds_read_b128 v[116:119], v181 offset:53248
	s_mov_b32 s28, s3
	s_nop 0
	v_and_or_b32 v18, v18, v177, s28
	v_med3_f32 v115, v132, v115, v18
	v_med3_f32 v136, v133, v132, v18
	v_med3_f32 v137, v134, v133, v18
	v_med3_f32 v18, v134, v18, s42
	s_waitcnt lgkmcnt(3)
	v_mfma_f32_32x32x16_f16 v[2:17], v[120:123], v[90:93], v[2:17]
	ds_read_b128 v[132:135], v181 offset:54272
	s_add_i32 s28, s3, 1
	s_nop 0
	v_and_or_b32 v19, v19, v177, s28
	v_med3_f32 v115, v136, v115, v19
	v_med3_f32 v136, v137, v136, v19
	v_med3_f32 v137, v18, v137, v19
	v_med3_f32 v18, v18, v19, s42
	s_waitcnt lgkmcnt(3)
	v_mfma_f32_32x32x16_f16 v[2:17], v[124:127], v[86:89], v[2:17]
	ds_read_b128 v[120:123], v181 offset:55296
	s_add_i32 s28, s3, 2
	s_nop 0
	v_and_or_b32 v19, v20, v177, s28
	v_med3_f32 v20, v136, v115, v19
	v_med3_f32 v115, v137, v136, v19
	v_med3_f32 v136, v18, v137, v19
	v_med3_f32 v18, v18, v19, s42
	s_waitcnt lgkmcnt(3)
	v_mfma_f32_32x32x16_f16 v[2:17], v[128:131], v[82:85], v[2:17]
	ds_read_b128 v[124:127], v181 offset:56320
	s_add_i32 s28, s3, 3
	s_nop 0
	v_and_or_b32 v19, v21, v177, s28
	v_med3_f32 v137, v115, v20, v19
	v_med3_f32 v115, v136, v115, v19
	v_med3_f32 v128, v18, v136, v19
	v_med3_f32 v129, v18, v19, s42
	s_waitcnt lgkmcnt(3)
	v_mfma_f32_32x32x16_f16 v[2:17], v[116:119], v[78:81], v[2:17]
	ds_read_b128 v[18:21], v181 offset:57344
	s_add_i32 s28, s3, 4
	s_nop 0
	v_and_or_b32 v22, v22, v177, s28
	v_med3_f32 v130, v115, v137, v22
	v_med3_f32 v115, v128, v115, v22
	v_med3_f32 v128, v129, v128, v22
	v_med3_f32 v22, v129, v22, s42
	s_waitcnt lgkmcnt(3)
	v_mfma_f32_32x32x16_f16 v[2:17], v[132:135], v[74:77], v[2:17]
	ds_read_b128 v[116:119], v181 offset:58368
	s_add_i32 s28, s3, 5
	s_nop 0
	v_and_or_b32 v23, v23, v177, s28
	v_med3_f32 v136, v115, v130, v23
	v_med3_f32 v115, v128, v115, v23
	v_med3_f32 v132, v22, v128, v23
	v_med3_f32 v22, v22, v23, s42
	s_waitcnt lgkmcnt(3)
	v_mfma_f32_32x32x16_f16 v[2:17], v[120:123], v[70:73], v[2:17]
	ds_read_b128 v[128:131], v181 offset:59392
	s_add_i32 s28, s3, 6
	s_nop 0
	v_and_or_b32 v23, v24, v177, s28
	v_med3_f32 v24, v115, v136, v23
	v_med3_f32 v115, v132, v115, v23
	v_med3_f32 v132, v22, v132, v23
	v_med3_f32 v22, v22, v23, s42
	s_waitcnt lgkmcnt(3)
	v_mfma_f32_32x32x16_f16 v[2:17], v[124:127], v[66:69], v[2:17]
	ds_read_b128 v[120:123], v181 offset:60416
	s_add_i32 s28, s3, 7
	s_nop 0
	v_and_or_b32 v23, v25, v177, s28
	v_med3_f32 v133, v115, v24, v23
	v_med3_f32 v115, v132, v115, v23
	v_med3_f32 v124, v22, v132, v23
	v_med3_f32 v125, v22, v23, s42
	s_waitcnt lgkmcnt(3)
	v_mfma_f32_32x32x16_f16 v[2:17], v[18:21], v[62:65], v[2:17]
	ds_read_b128 v[22:25], v181 offset:61440
	s_add_i32 s28, s3, 8
	s_nop 0
	v_and_or_b32 v26, v26, v177, s28
	v_med3_f32 v126, v115, v133, v26
	v_med3_f32 v115, v124, v115, v26
	v_med3_f32 v124, v125, v124, v26
	v_med3_f32 v26, v125, v26, s42
	s_waitcnt lgkmcnt(3)
	v_mfma_f32_32x32x16_f16 v[2:17], v[116:119], v[58:61], v[2:17]
	ds_read_b128 v[18:21], v181 offset:62464
	s_add_i32 s28, s3, 9
	s_nop 0
	v_and_or_b32 v27, v27, v177, s28
	v_med3_f32 v125, v115, v126, v27
	v_med3_f32 v115, v124, v115, v27
	v_med3_f32 v124, v26, v124, v27
	v_med3_f32 v26, v26, v27, s42
	s_waitcnt lgkmcnt(3)
	v_mfma_f32_32x32x16_f16 v[2:17], v[128:131], v[54:57], v[2:17]
	ds_read_b128 v[116:119], v181 offset:63488
	s_add_i32 s28, s3, 10
	s_nop 0
	v_and_or_b32 v27, v28, v177, s28
	v_med3_f32 v28, v115, v125, v27
	v_med3_f32 v115, v124, v115, v27
	v_med3_f32 v128, v26, v124, v27
	v_med3_f32 v26, v26, v27, s42
	s_waitcnt lgkmcnt(3)
	v_mfma_f32_32x32x16_f16 v[2:17], v[120:123], v[50:53], v[2:17]
	ds_read_b128 v[124:127], v181 offset:64512
	s_add_i32 s28, s3, 11
	s_nop 0
	v_and_or_b32 v27, v29, v177, s28
	v_med3_f32 v28, v115, v28, v27
	v_med3_f32 v29, v128, v115, v27
	v_med3_f32 v115, v26, v128, v27
	v_med3_f32 v26, v26, v27, s42
	s_waitcnt lgkmcnt(3)
	v_mfma_f32_32x32x16_f16 v[2:17], v[22:25], v[46:49], v[2:17]
	s_add_i32 s28, s3, 12
	s_nop 0
	v_and_or_b32 v27, v30, v177, s28
	v_med3_f32 v28, v29, v28, v27
	v_med3_f32 v29, v115, v29, v27
	v_med3_f32 v30, v26, v115, v27
	v_med3_f32 v22, v26, v27, s42
	s_waitcnt lgkmcnt(2)
	v_mfma_f32_32x32x16_f16 v[2:17], v[18:21], v[42:45], v[2:17]
	s_add_i32 s28, s3, 13
	s_nop 0
	v_and_or_b32 v23, v31, v177, s28
	v_med3_f32 v24, v29, v28, v23
	v_med3_f32 v25, v30, v29, v23
	v_med3_f32 v26, v22, v30, v23
	v_med3_f32 v18, v22, v23, s42
	s_waitcnt lgkmcnt(1)
	v_mfma_f32_32x32x16_f16 v[2:17], v[116:119], v[38:41], v[2:17]
	s_add_i32 s28, s3, 14
	s_nop 0
	v_and_or_b32 v19, v32, v177, s28
	v_med3_f32 v20, v25, v24, v19
	v_med3_f32 v21, v26, v25, v19
	v_med3_f32 v22, v18, v26, v19
	v_med3_f32 v18, v18, v19, s42
	s_waitcnt lgkmcnt(0)
	v_mfma_f32_32x32x16_f16 v[2:17], v[124:127], v[34:37], v[2:17]
	s_add_i32 s3, s3, 15
	s_nop 0
	v_and_or_b32 v19, v33, v177, s3
	v_med3_f32 v195, v21, v20, v19
	v_med3_f32 v196, v22, v21, v19
	v_med3_f32 v197, v18, v22, v19
	v_med3_f32 v198, v18, v19, s42
	s_add_i32 s3, s11, 16
	s_add_i32 s10, s10, 2
	s_add_i32 s11, s11, 64
	s_cmp_gt_u32 s10, 5
	v_add_u32_e32 v114, 0x200, v114
	s_cbranch_scc0 .Lrot_head
	s_barrier
	s_cmp_lg_u32 s40, 3
	v_and_b32_e32 v200, v2, v177
	v_and_b32_e32 v199, v3, v177
	v_and_b32_e32 v4, v4, v177
	s_mov_b64 s[10:11], -1
	s_cbranch_scc0 .LBB1_38
	s_movk_i32 s3, 0xf0
	v_cmp_gt_f32_e32 vcc, s41, v178
	v_or_b32_e32 v2, s3, v200
	s_movk_i32 s3, 0xf1
	v_med3_f32 v3, v196, v195, v2
	v_or_b32_e32 v20, s3, v199
	s_movk_i32 s3, 0xf2
	v_med3_f32 v18, v197, v196, v2
	v_med3_f32 v19, v198, v197, v2
	v_med3_f32 v2, v198, v2, s42
	v_med3_f32 v3, v18, v3, v20
	v_med3_f32 v18, v19, v18, v20
	v_med3_f32 v19, v2, v19, v20
	v_med3_f32 v2, v2, v20, s42
	v_or_b32_e32 v20, s3, v4
	s_movk_i32 s3, 0xf3
	v_med3_f32 v3, v18, v3, v20
	v_med3_f32 v18, v19, v18, v20
	v_med3_f32 v19, v2, v19, v20
	v_med3_f32 v2, v2, v20, s42
	v_and_or_b32 v20, v5, v177, s3
	s_movk_i32 s3, 0xf4
	v_med3_f32 v3, v18, v3, v20
	v_med3_f32 v18, v19, v18, v20
	v_med3_f32 v19, v2, v19, v20
	v_med3_f32 v2, v2, v20, s42
	v_and_or_b32 v20, v6, v177, s3
	s_movk_i32 s3, 0xf5
	v_med3_f32 v3, v18, v3, v20
	v_med3_f32 v18, v19, v18, v20
	v_med3_f32 v19, v2, v19, v20
	v_med3_f32 v2, v2, v20, s42
	v_and_or_b32 v20, v7, v177, s3
	s_movk_i32 s3, 0xf6
	v_med3_f32 v3, v18, v3, v20
	v_med3_f32 v18, v19, v18, v20
	v_med3_f32 v19, v2, v19, v20
	v_med3_f32 v2, v2, v20, s42
	v_and_or_b32 v20, v8, v177, s3
	s_movk_i32 s3, 0xf7
	v_med3_f32 v3, v18, v3, v20
	v_med3_f32 v18, v19, v18, v20
	v_med3_f32 v19, v2, v19, v20
	v_med3_f32 v2, v2, v20, s42
	v_and_or_b32 v20, v9, v177, s3
	s_movk_i32 s3, 0xf8
	v_med3_f32 v3, v18, v3, v20
	v_med3_f32 v18, v19, v18, v20
	v_med3_f32 v19, v2, v19, v20
	v_med3_f32 v2, v2, v20, s42
	v_and_or_b32 v20, v10, v177, s3
	s_movk_i32 s3, 0xf9
	v_med3_f32 v3, v18, v3, v20
	v_med3_f32 v18, v19, v18, v20
	v_med3_f32 v19, v2, v19, v20
	v_med3_f32 v2, v2, v20, s42
	v_and_or_b32 v20, v11, v177, s3
	s_movk_i32 s3, 0xfa
	v_med3_f32 v3, v18, v3, v20
	v_med3_f32 v18, v19, v18, v20
	v_med3_f32 v19, v2, v19, v20
	v_med3_f32 v2, v2, v20, s42
	v_and_or_b32 v20, v12, v177, s3
	s_movk_i32 s3, 0xfb
	v_med3_f32 v3, v18, v3, v20
	v_med3_f32 v18, v19, v18, v20
	v_med3_f32 v19, v2, v19, v20
	v_med3_f32 v2, v2, v20, s42
	v_and_or_b32 v20, v13, v177, s3
	s_movk_i32 s3, 0xfc
	v_med3_f32 v3, v18, v3, v20
	v_med3_f32 v18, v19, v18, v20
	v_med3_f32 v19, v2, v19, v20
	v_med3_f32 v2, v2, v20, s42
	v_and_or_b32 v20, v14, v177, s3
	s_movk_i32 s3, 0xfd
	v_med3_f32 v3, v18, v3, v20
	v_med3_f32 v18, v19, v18, v20
	v_med3_f32 v19, v2, v19, v20
	v_med3_f32 v2, v2, v20, s42
	v_and_or_b32 v20, v15, v177, s3
	s_movk_i32 s3, 0xfe
	v_med3_f32 v3, v18, v3, v20
	v_med3_f32 v18, v19, v18, v20
	v_med3_f32 v19, v2, v19, v20
	v_med3_f32 v2, v2, v20, s42
	v_and_or_b32 v20, v16, v177, s3
	s_movk_i32 s3, 0xff
	v_med3_f32 v3, v18, v3, v20
	v_med3_f32 v18, v19, v18, v20
	v_med3_f32 v19, v2, v19, v20
	v_med3_f32 v2, v2, v20, s42
	s_nop 0
	v_and_or_b32 v20, v17, v177, s3
	v_med3_f32 v3, v18, v3, v20
	v_med3_f32 v18, v19, v18, v20
	v_med3_f32 v19, v2, v19, v20
	v_med3_f32 v2, v2, v20, s42
	v_lshlrev_b32_e32 v20, 1, v2
	v_and_b32_e32 v20, 0x1f8, v20
	v_and_b32_e32 v2, 0xfffffe03, v2
	v_or3_b32 v2, v2, v20, v184
	v_lshlrev_b32_e32 v20, 1, v19
	v_and_b32_e32 v20, 0x1f8, v20
	v_and_b32_e32 v19, 0xfffffe03, v19
	v_or3_b32 v25, v19, v20, v184
	v_lshlrev_b32_e32 v19, 1, v18
	v_and_b32_e32 v19, 0x1f8, v19
	v_and_b32_e32 v18, 0xfffffe03, v18
	v_or3_b32 v18, v18, v19, v184
	v_lshlrev_b32_e32 v19, 1, v3
	v_and_b32_e32 v20, 0x1f8, v19
	ds_bpermute_b32 v19, v1, v2
	ds_bpermute_b32 v21, v1, v25
	ds_bpermute_b32 v22, v1, v18
	v_and_b32_e32 v3, 0xfffffe03, v3
	v_or3_b32 v20, v3, v20, v184
	s_waitcnt lgkmcnt(2)
	v_med3_f32 v24, v25, v18, v19
	v_med3_f32 v3, v2, v25, v19
	v_med3_f32 v2, v2, v19, s42
	s_waitcnt lgkmcnt(1)
	v_med3_f32 v25, v3, v24, v21
	v_med3_f32 v3, v2, v3, v21
	v_med3_f32 v2, v2, v21, s42
	s_waitcnt lgkmcnt(0)
	v_med3_f32 v27, v3, v25, v22
	v_med3_f32 v3, v2, v3, v22
	v_med3_f32 v26, v2, v22, s42
	v_mul_f32_e32 v2, 0x4f800000, v178
	v_cndmask_b32_e32 v28, v178, v2, vcc
	v_sqrt_f32_e32 v29, v28
	ds_bpermute_b32 v23, v1, v20
	v_add_u32_e32 v30, -1, v29
	v_fma_f32 v31, -v30, v29, v28
	v_cmp_ge_f32_e64 s[10:11], 0, v31
	v_add_u32_e32 v31, 1, v29
	s_waitcnt lgkmcnt(0)
	v_med3_f32 v2, v3, v27, v23
	v_cndmask_b32_e64 v30, v29, v30, s[10:11]
	v_fma_f32 v29, -v31, v29, v28
	v_cmp_lt_f32_e64 s[10:11], 0, v29
	v_med3_f32 v3, v26, v3, v23
	v_med3_f32 v26, v26, v23, s42
	v_cndmask_b32_e64 v29, v30, v31, s[10:11]
	v_mul_f32_e32 v30, 0x37800000, v29
	v_cndmask_b32_e32 v29, v29, v30, vcc
	v_cmp_class_f32_e32 vcc, v28, v179
	s_nop 1
	v_cndmask_b32_e32 v28, v29, v28, vcc
	v_mul_f32_e32 v28, v180, v28
	v_and_b32_e32 v29, 0x7fffffff, v26
	v_pk_mul_f32 v[28:29], v[28:29], s[24:25]
	s_nop 0
	v_add_f32_e32 v28, v28, v29
	v_sub_f32_e32 v29, v3, v26
	v_cmp_ngt_f32_e32 vcc, v29, v28
	v_mov_b32_e32 v29, 0
	s_and_saveexec_b64 s[10:11], vcc
	s_cbranch_execz .LBB1_13
	v_sub_f32_e32 v29, v2, v26
	v_cmp_ngt_f32_e32 vcc, v29, v28
	v_mov_b32_e32 v29, 1
	s_and_saveexec_b64 s[28:29], vcc
	v_med3_f32 v18, v18, v20, v19
	v_med3_f32 v18, v24, v18, v21
	v_med3_f32 v18, v25, v18, v22
	v_med3_f32 v18, v27, v18, v23
	v_sub_f32_e32 v18, v18, v26
	v_cmp_gt_f32_e32 vcc, v18, v28
	s_nop 1
	v_cndmask_b32_e64 v29, 3, 2, vcc
	s_or_b64 exec, exec, s[28:29]
